# iteration kernels: waves 4-7 enter phase 1 128 cycles after their SIMD partners (stagger)
# speedup vs baseline: 1.0115x; 1.0115x over previous
.Lffc_nocache:
	s_cmp_lt_u32 s27, 4
	s_cbranch_scc1 .Lffc_nostag
	s_sleep 2

.Lftc_nocache:
	s_cmp_lt_u32 s30, 4
	s_cbranch_scc1 .Lftc_nostag
	s_sleep 2
